# stack: P6 epilogue pipelined, P5 gate-row touches, P7 u2 pass pipelined, P11 final_g hoisted, GEMM DMA 4/4 rebalance in P2/P9/P10
# speedup vs baseline: 1.0044x; 1.0044x over previous
; #define LAS __attribute__((address_space(3)))
; __device__ __forceinline__ void p7_router(Frame& F, const Args& A, bool commit = true) {
;     ...
;         for (int i = 0; i < 4; ++i) { const int token = F.wave * 4 + i, m = t0 + token; const float rstd = rstdL[token];
;             const float* hr = H1 + (size_t)m * DM + 4 * F.lane; unsigned char* ur = WSP(unsigned char, WS_U) + (size_t)m * DM + 4 * F.lane;
; #pragma unroll
;             for (int j = 0; j < 8; ++j) { const f32x4 h = *(const f32x4*)(hr + 256 * j), g = *(const LAS f32x4*)(gainL + 4 * F.lane + 256 * j), s = *(const LAS f32x4*)(shiftL + 4 * F.lane + 256 * j);
;                 const f32x4 u = h * rstd * g + s; int w8 = __builtin_amdgcn_cvt_pk_fp8_f32(u.x, u.y, 0, false); w8 = __builtin_amdgcn_cvt_pk_fp8_f32(u.z, u.w, w8, true); *(int*)(ur + 256 * j) = w8; } }
.LBB0_889:
	s_or_b64 exec, exec, s[6:7]
	v_mov_b32_e32 v118, s1
	ds_read_b128 v[66:69], v118 offset:55424
	ds_read_b128 v[2:5], v99
	ds_read_b128 v[6:9], v99 offset:1024
	ds_read_b128 v[10:13], v99 offset:2048
	ds_read_b128 v[14:17], v99 offset:3072
	ds_read_b128 v[18:21], v99 offset:4096
	ds_read_b128 v[22:25], v99 offset:5120
	ds_read_b128 v[26:29], v99 offset:6144
	ds_read_b128 v[30:33], v99 offset:7168
	ds_read_b128 v[34:37], v99 offset:8192
	ds_read_b128 v[38:41], v99 offset:9216
	ds_read_b128 v[42:45], v99 offset:10240
	ds_read_b128 v[46:49], v99 offset:11264
	ds_read_b128 v[50:53], v99 offset:12288
	ds_read_b128 v[54:57], v99 offset:13312
	ds_read_b128 v[58:61], v99 offset:14336
	ds_read_b128 v[62:65], v99 offset:15360
	s_add_i32 s43, s43, s86
	v_add_u32_e32 v88, s11, v88
	s_mov_b64 s[70:71], 0x1000
	s_add_i32 s6, s0, s44
	s_ashr_i32 s7, s6, 31
	s_lshl_b64 s[46:47], s[6:7], 13
	s_lshl_b64 s[6:7], s[6:7], 11
	v_lshl_add_u64 v[206:207], v[76:77], 0, s[46:47]
	v_lshl_add_u64 v[210:211], v[78:79], 0, s[6:7]
	s_add_i32 s6, s2, s44
	s_ashr_i32 s7, s6, 31
	s_lshl_b64 s[46:47], s[6:7], 13
	s_lshl_b64 s[6:7], s[6:7], 11
	v_lshl_add_u64 v[212:213], v[76:77], 0, s[46:47]
	v_lshl_add_u64 v[216:217], v[78:79], 0, s[6:7]
	s_add_i32 s6, s3, s44
	s_ashr_i32 s7, s6, 31
	s_lshl_b64 s[46:47], s[6:7], 13
	s_lshl_b64 s[6:7], s[6:7], 11
	v_lshl_add_u64 v[218:219], v[76:77], 0, s[46:47]
	v_lshl_add_u64 v[222:223], v[78:79], 0, s[6:7]
	s_add_i32 s6, s10, s44
	s_ashr_i32 s7, s6, 31
	s_lshl_b64 s[46:47], s[6:7], 13
	s_lshl_b64 s[6:7], s[6:7], 11
	v_lshl_add_u64 v[224:225], v[76:77], 0, s[46:47]
	v_lshl_add_u64 v[228:229], v[78:79], 0, s[6:7]
	v_lshl_add_u64 v[208:209], v[206:207], 0, s[70:71]
	v_lshl_add_u64 v[214:215], v[212:213], 0, s[70:71]
	v_lshl_add_u64 v[220:221], v[218:219], 0, s[70:71]
	v_lshl_add_u64 v[226:227], v[224:225], 0, s[70:71]
	global_load_dwordx4 v[120:123], v[206:207], off
	global_load_dwordx4 v[124:127], v[206:207], off offset:1024
	global_load_dwordx4 v[128:131], v[206:207], off offset:2048
	global_load_dwordx4 v[132:135], v[206:207], off offset:3072
	global_load_dwordx4 v[136:139], v[208:209], off
	global_load_dwordx4 v[140:143], v[208:209], off offset:1024
	global_load_dwordx4 v[144:147], v[208:209], off offset:2048
	global_load_dwordx4 v[148:151], v[208:209], off offset:3072
	global_load_dwordx4 v[152:155], v[212:213], off
	global_load_dwordx4 v[156:159], v[212:213], off offset:1024
	global_load_dwordx4 v[160:163], v[212:213], off offset:2048
	global_load_dwordx4 v[164:167], v[212:213], off offset:3072
	global_load_dwordx4 v[168:171], v[214:215], off
	global_load_dwordx4 v[172:175], v[214:215], off offset:1024
	global_load_dwordx4 v[176:179], v[214:215], off offset:2048
	global_load_dwordx4 v[180:183], v[214:215], off offset:3072
	s_waitcnt vmcnt(15) lgkmcnt(0)
	v_pk_mul_f32 v[184:185], v[120:121], v[66:67] op_sel_hi:[1,0]
	v_pk_mul_f32 v[186:187], v[122:123], v[66:67] op_sel_hi:[1,0]
	v_pk_fma_f32 v[184:185], v[184:185], v[2:3], v[34:35]
	v_pk_fma_f32 v[186:187], v[186:187], v[4:5], v[36:37]
	s_nop 0
	v_cvt_pk_fp8_f32 v188, v184, v185
	v_cvt_pk_fp8_f32 v188, v186, v187 op_sel:[0,0,1]
	global_store_dword v[210:211], v188, off
	global_load_dwordx4 v[120:123], v[218:219], off
	s_waitcnt vmcnt(16)
	v_pk_mul_f32 v[184:185], v[124:125], v[66:67] op_sel_hi:[1,0]
	v_pk_mul_f32 v[186:187], v[126:127], v[66:67] op_sel_hi:[1,0]
	v_pk_fma_f32 v[184:185], v[184:185], v[6:7], v[38:39]
	v_pk_fma_f32 v[186:187], v[186:187], v[8:9], v[40:41]
	s_nop 0
	v_cvt_pk_fp8_f32 v188, v184, v185
	v_cvt_pk_fp8_f32 v188, v186, v187 op_sel:[0,0,1]
	global_store_dword v[210:211], v188, off offset:256
	global_load_dwordx4 v[124:127], v[218:219], off offset:1024
	s_waitcnt vmcnt(17)
	v_pk_mul_f32 v[184:185], v[128:129], v[66:67] op_sel_hi:[1,0]
	v_pk_mul_f32 v[186:187], v[130:131], v[66:67] op_sel_hi:[1,0]
	v_pk_fma_f32 v[184:185], v[184:185], v[10:11], v[42:43]
	v_pk_fma_f32 v[186:187], v[186:187], v[12:13], v[44:45]
	s_nop 0
	v_cvt_pk_fp8_f32 v188, v184, v185
	v_cvt_pk_fp8_f32 v188, v186, v187 op_sel:[0,0,1]
	global_store_dword v[210:211], v188, off offset:512
	global_load_dwordx4 v[128:131], v[218:219], off offset:2048
	s_waitcnt vmcnt(18)
	v_pk_mul_f32 v[184:185], v[132:133], v[66:67] op_sel_hi:[1,0]
	v_pk_mul_f32 v[186:187], v[134:135], v[66:67] op_sel_hi:[1,0]
	v_pk_fma_f32 v[184:185], v[184:185], v[14:15], v[46:47]
	v_pk_fma_f32 v[186:187], v[186:187], v[16:17], v[48:49]
	s_nop 0
	v_cvt_pk_fp8_f32 v188, v184, v185
	v_cvt_pk_fp8_f32 v188, v186, v187 op_sel:[0,0,1]
	global_store_dword v[210:211], v188, off offset:768
	global_load_dwordx4 v[132:135], v[218:219], off offset:3072
	s_waitcnt vmcnt(19)
	v_pk_mul_f32 v[184:185], v[136:137], v[66:67] op_sel_hi:[1,0]
	v_pk_mul_f32 v[186:187], v[138:139], v[66:67] op_sel_hi:[1,0]
	v_pk_fma_f32 v[184:185], v[184:185], v[18:19], v[50:51]
	v_pk_fma_f32 v[186:187], v[186:187], v[20:21], v[52:53]
	s_nop 0
	v_cvt_pk_fp8_f32 v188, v184, v185
	v_cvt_pk_fp8_f32 v188, v186, v187 op_sel:[0,0,1]
	global_store_dword v[210:211], v188, off offset:1024
	global_load_dwordx4 v[136:139], v[220:221], off
	s_waitcnt vmcnt(20)
	v_pk_mul_f32 v[184:185], v[140:141], v[66:67] op_sel_hi:[1,0]
	v_pk_mul_f32 v[186:187], v[142:143], v[66:67] op_sel_hi:[1,0]
	v_pk_fma_f32 v[184:185], v[184:185], v[22:23], v[54:55]
	v_pk_fma_f32 v[186:187], v[186:187], v[24:25], v[56:57]
	s_nop 0
	v_cvt_pk_fp8_f32 v188, v184, v185
	v_cvt_pk_fp8_f32 v188, v186, v187 op_sel:[0,0,1]
	global_store_dword v[210:211], v188, off offset:1280
	global_load_dwordx4 v[140:143], v[220:221], off offset:1024
	s_waitcnt vmcnt(21)
; #define LAS __attribute__((address_space(3)))
; __device__ __forceinline__ void p7_router(Frame& F, const Args& A, bool commit = true) {
;     ...
;         for (int i = 0; i < 4; ++i) { const int token = F.wave * 4 + i, m = t0 + token; const float rstd = rstdL[token];
;             const float* hr = H1 + (size_t)m * DM + 4 * F.lane; unsigned char* ur = WSP(unsigned char, WS_U) + (size_t)m * DM + 4 * F.lane;
; #pragma unroll
;             for (int j = 0; j < 8; ++j) { const f32x4 h = *(const f32x4*)(hr + 256 * j), g = *(const LAS f32x4*)(gainL + 4 * F.lane + 256 * j), s = *(const LAS f32x4*)(shiftL + 4 * F.lane + 256 * j);
;                 const f32x4 u = h * rstd * g + s; int w8 = __builtin_amdgcn_cvt_pk_fp8_f32(u.x, u.y, 0, false); w8 = __builtin_amdgcn_cvt_pk_fp8_f32(u.z, u.w, w8, true); *(int*)(ur + 256 * j) = w8; } }
	v_pk_mul_f32 v[184:185], v[144:145], v[66:67] op_sel_hi:[1,0]
	v_pk_mul_f32 v[186:187], v[146:147], v[66:67] op_sel_hi:[1,0]
	v_pk_fma_f32 v[184:185], v[184:185], v[26:27], v[58:59]
	v_pk_fma_f32 v[186:187], v[186:187], v[28:29], v[60:61]
	s_nop 0
	v_cvt_pk_fp8_f32 v188, v184, v185
	v_cvt_pk_fp8_f32 v188, v186, v187 op_sel:[0,0,1]
	global_store_dword v[210:211], v188, off offset:1536
	global_load_dwordx4 v[144:147], v[220:221], off offset:2048
	s_waitcnt vmcnt(22)
	v_pk_mul_f32 v[184:185], v[148:149], v[66:67] op_sel_hi:[1,0]
	v_pk_mul_f32 v[186:187], v[150:151], v[66:67] op_sel_hi:[1,0]
	v_pk_fma_f32 v[184:185], v[184:185], v[30:31], v[62:63]
	v_pk_fma_f32 v[186:187], v[186:187], v[32:33], v[64:65]
	s_nop 0
	v_cvt_pk_fp8_f32 v188, v184, v185
	v_cvt_pk_fp8_f32 v188, v186, v187 op_sel:[0,0,1]
	global_store_dword v[210:211], v188, off offset:1792
	global_load_dwordx4 v[148:151], v[220:221], off offset:3072
	s_waitcnt vmcnt(23)
	v_pk_mul_f32 v[184:185], v[152:153], v[66:67] op_sel:[0,1]
	v_pk_mul_f32 v[186:187], v[154:155], v[66:67] op_sel:[0,1]
	v_pk_fma_f32 v[184:185], v[184:185], v[2:3], v[34:35]
	v_pk_fma_f32 v[186:187], v[186:187], v[4:5], v[36:37]
	s_nop 0
	v_cvt_pk_fp8_f32 v188, v184, v185
	v_cvt_pk_fp8_f32 v188, v186, v187 op_sel:[0,0,1]
	global_store_dword v[216:217], v188, off
	global_load_dwordx4 v[152:155], v[224:225], off
	s_waitcnt vmcnt(24)
	v_pk_mul_f32 v[184:185], v[156:157], v[66:67] op_sel:[0,1]
	v_pk_mul_f32 v[186:187], v[158:159], v[66:67] op_sel:[0,1]
	v_pk_fma_f32 v[184:185], v[184:185], v[6:7], v[38:39]
	v_pk_fma_f32 v[186:187], v[186:187], v[8:9], v[40:41]
	s_nop 0
	v_cvt_pk_fp8_f32 v188, v184, v185
	v_cvt_pk_fp8_f32 v188, v186, v187 op_sel:[0,0,1]
	global_store_dword v[216:217], v188, off offset:256
	global_load_dwordx4 v[156:159], v[224:225], off offset:1024
	s_waitcnt vmcnt(25)
	v_pk_mul_f32 v[184:185], v[160:161], v[66:67] op_sel:[0,1]
	v_pk_mul_f32 v[186:187], v[162:163], v[66:67] op_sel:[0,1]
	v_pk_fma_f32 v[184:185], v[184:185], v[10:11], v[42:43]
	v_pk_fma_f32 v[186:187], v[186:187], v[12:13], v[44:45]
	s_nop 0
	v_cvt_pk_fp8_f32 v188, v184, v185
	v_cvt_pk_fp8_f32 v188, v186, v187 op_sel:[0,0,1]
	global_store_dword v[216:217], v188, off offset:512
	global_load_dwordx4 v[160:163], v[224:225], off offset:2048
	s_waitcnt vmcnt(26)
	v_pk_mul_f32 v[184:185], v[164:165], v[66:67] op_sel:[0,1]
	v_pk_mul_f32 v[186:187], v[166:167], v[66:67] op_sel:[0,1]
	v_pk_fma_f32 v[184:185], v[184:185], v[14:15], v[46:47]
	v_pk_fma_f32 v[186:187], v[186:187], v[16:17], v[48:49]
	s_nop 0
	v_cvt_pk_fp8_f32 v188, v184, v185
	v_cvt_pk_fp8_f32 v188, v186, v187 op_sel:[0,0,1]
	global_store_dword v[216:217], v188, off offset:768
	global_load_dwordx4 v[164:167], v[224:225], off offset:3072
	s_waitcnt vmcnt(27)
	v_pk_mul_f32 v[184:185], v[168:169], v[66:67] op_sel:[0,1]
	v_pk_mul_f32 v[186:187], v[170:171], v[66:67] op_sel:[0,1]
	v_pk_fma_f32 v[184:185], v[184:185], v[18:19], v[50:51]
	v_pk_fma_f32 v[186:187], v[186:187], v[20:21], v[52:53]
	s_nop 0
	v_cvt_pk_fp8_f32 v188, v184, v185
	v_cvt_pk_fp8_f32 v188, v186, v187 op_sel:[0,0,1]
	global_store_dword v[216:217], v188, off offset:1024
	global_load_dwordx4 v[168:171], v[226:227], off
	s_waitcnt vmcnt(28)
	v_pk_mul_f32 v[184:185], v[172:173], v[66:67] op_sel:[0,1]
	v_pk_mul_f32 v[186:187], v[174:175], v[66:67] op_sel:[0,1]
	v_pk_fma_f32 v[184:185], v[184:185], v[22:23], v[54:55]
	v_pk_fma_f32 v[186:187], v[186:187], v[24:25], v[56:57]
	s_nop 0
	v_cvt_pk_fp8_f32 v188, v184, v185
	v_cvt_pk_fp8_f32 v188, v186, v187 op_sel:[0,0,1]
	global_store_dword v[216:217], v188, off offset:1280
	global_load_dwordx4 v[172:175], v[226:227], off offset:1024
	s_waitcnt vmcnt(29)
	v_pk_mul_f32 v[184:185], v[176:177], v[66:67] op_sel:[0,1]
	v_pk_mul_f32 v[186:187], v[178:179], v[66:67] op_sel:[0,1]
	v_pk_fma_f32 v[184:185], v[184:185], v[26:27], v[58:59]
	v_pk_fma_f32 v[186:187], v[186:187], v[28:29], v[60:61]
	s_nop 0
	v_cvt_pk_fp8_f32 v188, v184, v185
	v_cvt_pk_fp8_f32 v188, v186, v187 op_sel:[0,0,1]
	global_store_dword v[216:217], v188, off offset:1536
	global_load_dwordx4 v[176:179], v[226:227], off offset:2048
	s_waitcnt vmcnt(30)
	v_pk_mul_f32 v[184:185], v[180:181], v[66:67] op_sel:[0,1]
	v_pk_mul_f32 v[186:187], v[182:183], v[66:67] op_sel:[0,1]
	v_pk_fma_f32 v[184:185], v[184:185], v[30:31], v[62:63]
	v_pk_fma_f32 v[186:187], v[186:187], v[32:33], v[64:65]
	s_nop 0
	v_cvt_pk_fp8_f32 v188, v184, v185
	v_cvt_pk_fp8_f32 v188, v186, v187 op_sel:[0,0,1]
	global_store_dword v[216:217], v188, off offset:1792
	global_load_dwordx4 v[180:183], v[226:227], off offset:3072
	s_waitcnt vmcnt(30)
	v_pk_mul_f32 v[184:185], v[120:121], v[68:69] op_sel_hi:[1,0]
	v_pk_mul_f32 v[186:187], v[122:123], v[68:69] op_sel_hi:[1,0]
	v_pk_fma_f32 v[184:185], v[184:185], v[2:3], v[34:35]
	v_pk_fma_f32 v[186:187], v[186:187], v[4:5], v[36:37]
	s_nop 0
	v_cvt_pk_fp8_f32 v188, v184, v185
	v_cvt_pk_fp8_f32 v188, v186, v187 op_sel:[0,0,1]
	global_store_dword v[222:223], v188, off
	s_waitcnt vmcnt(29)
	v_pk_mul_f32 v[184:185], v[124:125], v[68:69] op_sel_hi:[1,0]
	v_pk_mul_f32 v[186:187], v[126:127], v[68:69] op_sel_hi:[1,0]
	v_pk_fma_f32 v[184:185], v[184:185], v[6:7], v[38:39]
	v_pk_fma_f32 v[186:187], v[186:187], v[8:9], v[40:41]
	s_nop 0
	v_cvt_pk_fp8_f32 v188, v184, v185
	v_cvt_pk_fp8_f32 v188, v186, v187 op_sel:[0,0,1]
	global_store_dword v[222:223], v188, off offset:256
	s_waitcnt vmcnt(28)
; #define LAS __attribute__((address_space(3)))
; __device__ __forceinline__ void p7_router(Frame& F, const Args& A, bool commit = true) {
;     ...
;         for (int i = 0; i < 4; ++i) { const int token = F.wave * 4 + i, m = t0 + token; const float rstd = rstdL[token];
;             const float* hr = H1 + (size_t)m * DM + 4 * F.lane; unsigned char* ur = WSP(unsigned char, WS_U) + (size_t)m * DM + 4 * F.lane;
; #pragma unroll
;             for (int j = 0; j < 8; ++j) { const f32x4 h = *(const f32x4*)(hr + 256 * j), g = *(const LAS f32x4*)(gainL + 4 * F.lane + 256 * j), s = *(const LAS f32x4*)(shiftL + 4 * F.lane + 256 * j);
;                 const f32x4 u = h * rstd * g + s; int w8 = __builtin_amdgcn_cvt_pk_fp8_f32(u.x, u.y, 0, false); w8 = __builtin_amdgcn_cvt_pk_fp8_f32(u.z, u.w, w8, true); *(int*)(ur + 256 * j) = w8; } }
;         __syncthreads();
	v_pk_mul_f32 v[184:185], v[128:129], v[68:69] op_sel_hi:[1,0]
	v_pk_mul_f32 v[186:187], v[130:131], v[68:69] op_sel_hi:[1,0]
	v_pk_fma_f32 v[184:185], v[184:185], v[10:11], v[42:43]
	v_pk_fma_f32 v[186:187], v[186:187], v[12:13], v[44:45]
	s_nop 0
	v_cvt_pk_fp8_f32 v188, v184, v185
	v_cvt_pk_fp8_f32 v188, v186, v187 op_sel:[0,0,1]
	global_store_dword v[222:223], v188, off offset:512
	s_waitcnt vmcnt(27)
	v_pk_mul_f32 v[184:185], v[132:133], v[68:69] op_sel_hi:[1,0]
	v_pk_mul_f32 v[186:187], v[134:135], v[68:69] op_sel_hi:[1,0]
	v_pk_fma_f32 v[184:185], v[184:185], v[14:15], v[46:47]
	v_pk_fma_f32 v[186:187], v[186:187], v[16:17], v[48:49]
	s_nop 0
	v_cvt_pk_fp8_f32 v188, v184, v185
	v_cvt_pk_fp8_f32 v188, v186, v187 op_sel:[0,0,1]
	global_store_dword v[222:223], v188, off offset:768
	s_waitcnt vmcnt(26)
	v_pk_mul_f32 v[184:185], v[136:137], v[68:69] op_sel_hi:[1,0]
	v_pk_mul_f32 v[186:187], v[138:139], v[68:69] op_sel_hi:[1,0]
	v_pk_fma_f32 v[184:185], v[184:185], v[18:19], v[50:51]
	v_pk_fma_f32 v[186:187], v[186:187], v[20:21], v[52:53]
	s_nop 0
	v_cvt_pk_fp8_f32 v188, v184, v185
	v_cvt_pk_fp8_f32 v188, v186, v187 op_sel:[0,0,1]
	global_store_dword v[222:223], v188, off offset:1024
	s_waitcnt vmcnt(25)
	v_pk_mul_f32 v[184:185], v[140:141], v[68:69] op_sel_hi:[1,0]
	v_pk_mul_f32 v[186:187], v[142:143], v[68:69] op_sel_hi:[1,0]
	v_pk_fma_f32 v[184:185], v[184:185], v[22:23], v[54:55]
	v_pk_fma_f32 v[186:187], v[186:187], v[24:25], v[56:57]
	s_nop 0
	v_cvt_pk_fp8_f32 v188, v184, v185
	v_cvt_pk_fp8_f32 v188, v186, v187 op_sel:[0,0,1]
	global_store_dword v[222:223], v188, off offset:1280
	s_waitcnt vmcnt(24)
	v_pk_mul_f32 v[184:185], v[144:145], v[68:69] op_sel_hi:[1,0]
	v_pk_mul_f32 v[186:187], v[146:147], v[68:69] op_sel_hi:[1,0]
	v_pk_fma_f32 v[184:185], v[184:185], v[26:27], v[58:59]
	v_pk_fma_f32 v[186:187], v[186:187], v[28:29], v[60:61]
	s_nop 0
	v_cvt_pk_fp8_f32 v188, v184, v185
	v_cvt_pk_fp8_f32 v188, v186, v187 op_sel:[0,0,1]
	global_store_dword v[222:223], v188, off offset:1536
	s_waitcnt vmcnt(23)
	v_pk_mul_f32 v[184:185], v[148:149], v[68:69] op_sel_hi:[1,0]
	v_pk_mul_f32 v[186:187], v[150:151], v[68:69] op_sel_hi:[1,0]
	v_pk_fma_f32 v[184:185], v[184:185], v[30:31], v[62:63]
	v_pk_fma_f32 v[186:187], v[186:187], v[32:33], v[64:65]
	s_nop 0
	v_cvt_pk_fp8_f32 v188, v184, v185
	v_cvt_pk_fp8_f32 v188, v186, v187 op_sel:[0,0,1]
	global_store_dword v[222:223], v188, off offset:1792
	s_waitcnt vmcnt(22)
	v_pk_mul_f32 v[184:185], v[152:153], v[68:69] op_sel:[0,1]
	v_pk_mul_f32 v[186:187], v[154:155], v[68:69] op_sel:[0,1]
	v_pk_fma_f32 v[184:185], v[184:185], v[2:3], v[34:35]
	v_pk_fma_f32 v[186:187], v[186:187], v[4:5], v[36:37]
	s_nop 0
	v_cvt_pk_fp8_f32 v188, v184, v185
	v_cvt_pk_fp8_f32 v188, v186, v187 op_sel:[0,0,1]
	global_store_dword v[228:229], v188, off
	s_waitcnt vmcnt(21)
	v_pk_mul_f32 v[184:185], v[156:157], v[68:69] op_sel:[0,1]
	v_pk_mul_f32 v[186:187], v[158:159], v[68:69] op_sel:[0,1]
	v_pk_fma_f32 v[184:185], v[184:185], v[6:7], v[38:39]
	v_pk_fma_f32 v[186:187], v[186:187], v[8:9], v[40:41]
	s_nop 0
	v_cvt_pk_fp8_f32 v188, v184, v185
	v_cvt_pk_fp8_f32 v188, v186, v187 op_sel:[0,0,1]
	global_store_dword v[228:229], v188, off offset:256
	s_waitcnt vmcnt(20)
	v_pk_mul_f32 v[184:185], v[160:161], v[68:69] op_sel:[0,1]
	v_pk_mul_f32 v[186:187], v[162:163], v[68:69] op_sel:[0,1]
	v_pk_fma_f32 v[184:185], v[184:185], v[10:11], v[42:43]
	v_pk_fma_f32 v[186:187], v[186:187], v[12:13], v[44:45]
	s_nop 0
	v_cvt_pk_fp8_f32 v188, v184, v185
	v_cvt_pk_fp8_f32 v188, v186, v187 op_sel:[0,0,1]
	global_store_dword v[228:229], v188, off offset:512
	s_waitcnt vmcnt(19)
	v_pk_mul_f32 v[184:185], v[164:165], v[68:69] op_sel:[0,1]
	v_pk_mul_f32 v[186:187], v[166:167], v[68:69] op_sel:[0,1]
	v_pk_fma_f32 v[184:185], v[184:185], v[14:15], v[46:47]
	v_pk_fma_f32 v[186:187], v[186:187], v[16:17], v[48:49]
	s_nop 0
	v_cvt_pk_fp8_f32 v188, v184, v185
	v_cvt_pk_fp8_f32 v188, v186, v187 op_sel:[0,0,1]
	global_store_dword v[228:229], v188, off offset:768
	s_waitcnt vmcnt(18)
	v_pk_mul_f32 v[184:185], v[168:169], v[68:69] op_sel:[0,1]
	v_pk_mul_f32 v[186:187], v[170:171], v[68:69] op_sel:[0,1]
	v_pk_fma_f32 v[184:185], v[184:185], v[18:19], v[50:51]
	v_pk_fma_f32 v[186:187], v[186:187], v[20:21], v[52:53]
	s_nop 0
	v_cvt_pk_fp8_f32 v188, v184, v185
	v_cvt_pk_fp8_f32 v188, v186, v187 op_sel:[0,0,1]
	global_store_dword v[228:229], v188, off offset:1024
	s_waitcnt vmcnt(17)
	v_pk_mul_f32 v[184:185], v[172:173], v[68:69] op_sel:[0,1]
	v_pk_mul_f32 v[186:187], v[174:175], v[68:69] op_sel:[0,1]
	v_pk_fma_f32 v[184:185], v[184:185], v[22:23], v[54:55]
	v_pk_fma_f32 v[186:187], v[186:187], v[24:25], v[56:57]
	s_nop 0
	v_cvt_pk_fp8_f32 v188, v184, v185
	v_cvt_pk_fp8_f32 v188, v186, v187 op_sel:[0,0,1]
	global_store_dword v[228:229], v188, off offset:1280
	s_waitcnt vmcnt(16)
	v_pk_mul_f32 v[184:185], v[176:177], v[68:69] op_sel:[0,1]
	v_pk_mul_f32 v[186:187], v[178:179], v[68:69] op_sel:[0,1]
	v_pk_fma_f32 v[184:185], v[184:185], v[26:27], v[58:59]
	v_pk_fma_f32 v[186:187], v[186:187], v[28:29], v[60:61]
	s_nop 0
	v_cvt_pk_fp8_f32 v188, v184, v185
	v_cvt_pk_fp8_f32 v188, v186, v187 op_sel:[0,0,1]
	global_store_dword v[228:229], v188, off offset:1536
	s_waitcnt vmcnt(15)
	v_pk_mul_f32 v[184:185], v[180:181], v[68:69] op_sel:[0,1]
	v_pk_mul_f32 v[186:187], v[182:183], v[68:69] op_sel:[0,1]
	v_pk_fma_f32 v[184:185], v[184:185], v[30:31], v[62:63]
	v_pk_fma_f32 v[186:187], v[186:187], v[32:33], v[64:65]
	s_nop 0
	v_cvt_pk_fp8_f32 v188, v184, v185
	v_cvt_pk_fp8_f32 v188, v186, v187 op_sel:[0,0,1]
	global_store_dword v[228:229], v188, off offset:1792
	s_cmpk_lt_i32 s43, 0x100
	s_barrier
	s_cbranch_scc0 .LBB0_908

; __device__ __forceinline__ void p11_final(Frame& F, const Args& A) {
;     ...
;     for (int m = gw; m < T; m += NGW) {
;         const int bb = m / SEQ; const bf16* yr[4]; float p[4];
; #pragma unroll
;         for (int k = 0; k < 4; ++k) { const int e = WSP(int, WS_TOPI)[m * 4 + k], pos = WSP(int, WS_POS)[m * 4 + k]; p[k] = WSP(float, WS_TOPP)[m * 4 + k];
;             yr[k] = WSP(bf16, WS_YSLOT) + ((size_t)ts[e] * 256 + pos) * DM + 4 * F.lane; }
;         const float* hr = WSP(float, WS_H1) + (size_t)m * DM + 4 * F.lane; f32x4 v[8]; float s = 0.f;
; #pragma unroll
.LBB0_1147:
	s_or_b64 exec, exec, s[0:1]
	s_lshl_b32 s0, s90, 3
	v_readlane_b32 s1, v246, 40
	s_add_i32 s2, s0, s1
	s_cmpk_gt_i32 s2, 0x1fff
	s_waitcnt vmcnt(0) lgkmcnt(0)
	s_barrier
	s_cbranch_scc1 .LBB0_1150
	v_lshlrev_b32_e32 v0, 2, v1
	v_lshlrev_b32_e32 v68, 4, v1
	v_mbcnt_hi_u32_b32 v1, -1, v190
	v_and_b32_e32 v2, 64, v1
	v_add_u32_e32 v2, 64, v2
	v_xor_b32_e32 v3, 1, v1
	v_cmp_lt_i32_e32 vcc, v3, v2
	s_lshl_b32 s4, s86, 3
	s_add_u32 s18, s30, 0x200000
	v_cndmask_b32_e32 v3, v1, v3, vcc
	v_lshlrev_b32_e32 v87, 2, v3
	v_xor_b32_e32 v3, 2, v1
	s_addc_u32 s19, s31, 0
	v_cmp_lt_i32_e32 vcc, v3, v2
	s_add_u32 s20, s30, 0x280000
	s_addc_u32 s21, s31, 0
	v_cndmask_b32_e32 v3, v1, v3, vcc
	v_mov_b32_e32 v69, 0
	v_lshlrev_b32_e32 v89, 2, v3
	v_xor_b32_e32 v3, 4, v1
	s_add_u32 s22, s30, 0x240000
	v_lshl_add_u64 v[70:71], s[26:27], 0, v[68:69]
	s_mov_b64 s[0:1], 0x1000
	v_cmp_lt_i32_e32 vcc, v3, v2
	s_addc_u32 s23, s31, 0
	v_lshl_add_u64 v[72:73], v[70:71], 0, s[0:1]
	s_mov_b64 s[0:1], 0x1400
	v_cndmask_b32_e32 v3, v1, v3, vcc
	s_add_u32 s6, s30, 0x3a200000
	v_lshl_add_u64 v[74:75], v[70:71], 0, s[0:1]
	s_mov_b64 s[0:1], 0x1800
	v_lshlrev_b32_e32 v90, 2, v3
	v_xor_b32_e32 v3, 8, v1
	s_addc_u32 s7, s31, 0
	v_lshl_add_u64 v[76:77], v[70:71], 0, s[0:1]
	s_mov_b64 s[0:1], 0x1c00
	v_cmp_lt_i32_e32 vcc, v3, v2
	s_ashr_i32 s3, s2, 31
	v_lshl_add_u64 v[78:79], v[70:71], 0, s[0:1]
	v_cndmask_b32_e32 v3, v1, v3, vcc
	s_lshl_b64 s[0:1], s[2:3], 13
	v_lshlrev_b32_e32 v91, 2, v3
	v_xor_b32_e32 v3, 16, v1
	s_add_u32 s8, s30, s0
	v_cmp_lt_i32_e32 vcc, v3, v2
	s_addc_u32 s9, s31, s1
	s_ashr_i32 s5, s4, 31
	v_cndmask_b32_e32 v3, v1, v3, vcc
	s_lshl_b64 s[10:11], s[4:5], 13
	v_lshlrev_b32_e32 v92, 2, v3
	v_xor_b32_e32 v3, 32, v1
	s_add_u32 s12, s28, s0
	v_cmp_lt_i32_e32 vcc, v3, v2
	s_addc_u32 s13, s29, s1
	v_readlane_b32 s1, v246, 40
	v_cndmask_b32_e32 v1, v1, v3, vcc
	s_lshl_b32 s0, s90, 5
	s_lshl_b32 s1, s1, 2
	v_lshlrev_b32_e32 v93, 2, v1
	s_add_i32 s14, s0, s1
	s_lshl_b32 s3, s86, 5
	s_add_i32 s5, 0, 0x27400
	v_lshlrev_b32_e32 v94, 1, v0
	v_lshlrev_b32_e32 v80, 2, v0
	v_mov_b32_e32 v81, v69
	s_mov_b64 s[16:17], 0x10a000
	s_mov_b32 s24, 0x22200000
	s_mov_b32 s25, 0x10b000
	s_mov_b32 s26, 0x22201000
	v_mov_b32_e32 v95, 0x3727c5ac
	s_mov_b32 s27, 0xf800000
	v_mov_b32_e32 v96, 0x260
	s_movk_i32 s28, 0x1000
	global_load_dwordx4 v[226:229], v[70:71], off
	global_load_dwordx4 v[230:233], v[70:71], off offset:1024
	global_load_dwordx4 v[234:237], v[70:71], off offset:2048
	global_load_dwordx4 v[238:241], v[70:71], off offset:3072
	global_load_dwordx4 v[242:245], v[72:73], off
	global_load_dwordx4 v[248:251], v[74:75], off
	global_load_dwordx4 v[252:255], v[76:77], off
	global_load_dwordx4 v[0:3], v[78:79], off
	s_waitcnt vmcnt(0)
.LBB0_1149:
	s_ashr_i32 s15, s14, 31
	v_lshl_add_u64 v[4:5], s[8:9], 0, v[68:69]
	s_lshl_b64 s[0:1], s[14:15], 2
	v_add_co_u32_e32 v36, vcc, s24, v4
	s_add_u32 s34, s18, s0
	s_nop 0
	v_addc_co_u32_e32 v37, vcc, 0, v5, vcc
	v_add_co_u32_e32 v38, vcc, s26, v4
	s_addc_u32 s35, s19, s1
	v_addc_co_u32_e32 v39, vcc, 0, v5, vcc
	global_load_dwordx4 v[28:31], v[36:37], off offset:1024
	global_load_dwordx4 v[24:27], v[36:37], off offset:2048
	global_load_dwordx4 v[16:19], v[36:37], off offset:3072
	global_load_dwordx4 v[32:35], v[38:39], off offset:-4096
	global_load_dwordx4 v[20:23], v[38:39], off
	global_load_dwordx4 v[12:15], v[38:39], off offset:1024
	global_load_dwordx4 v[8:11], v[38:39], off offset:2048
	global_load_dwordx4 v[4:7], v[38:39], off offset:3072
	global_load_dwordx4 v[98:101], v69, s[34:35]
	s_add_u32 s34, s20, s0
	s_addc_u32 s35, s21, s1
	s_add_u32 s0, s22, s0
	s_addc_u32 s1, s23, s1
	global_load_dword v106, v69, s[34:35]
	global_load_dword v88, v69, s[0:1]
	s_add_i32 s34, s14, 1
	s_ashr_i32 s35, s34, 31
	s_lshl_b64 s[0:1], s[34:35], 2
	s_add_u32 s34, s20, s0
	s_addc_u32 s35, s21, s1
	global_load_dwordx3 v[102:104], v69, s[34:35]
	s_add_u32 s0, s22, s0
	s_addc_u32 s1, s23, s1
	global_load_dword v86, v69, s[0:1]
	s_add_i32 s34, s14, 2
	s_ashr_i32 s35, s34, 31
	s_lshl_b64 s[0:1], s[34:35], 2
	s_add_u32 s0, s22, s0
	s_addc_u32 s1, s23, s1
	s_ashr_i32 s15, s2, 31
	global_load_dwordx2 v[84:85], v69, s[0:1]
	s_lshr_b32 s0, s15, 20
	s_add_i32 s0, s2, s0
	s_lshr_b32 s0, s0, 12
	s_mulk_i32 s0, 0x3000
	s_ashr_i32 s1, s0, 31
	s_lshl_b64 s[0:1], s[0:1], 2
	s_add_u32 s0, s30, s0
	s_addc_u32 s1, s31, s1
	v_lshl_add_u64 v[36:37], s[0:1], 0, v[80:81]
	v_lshl_add_u64 v[108:109], v[36:37], 0, s[16:17]
	v_add_co_u32_e32 v110, vcc, s25, v36
	v_lshl_add_u64 v[82:83], s[12:13], 0, v[68:69]
	s_nop 0
	v_addc_co_u32_e32 v111, vcc, 0, v37, vcc
	global_load_dwordx4 v[60:63], v[108:109], off offset:1024
	global_load_dwordx4 v[56:59], v[108:109], off offset:2048
	global_load_dwordx4 v[48:51], v[108:109], off offset:3072
	global_load_dwordx4 v[64:67], v[110:111], off offset:-4096
	global_load_dwordx4 v[52:55], v[110:111], off
	global_load_dwordx4 v[44:47], v[110:111], off offset:1024
	global_load_dwordx4 v[40:43], v[110:111], off offset:2048
	global_load_dwordx4 v[36:39], v[110:111], off offset:3072
	s_add_i32 s2, s2, s4
	s_add_u32 s8, s8, s10
	s_addc_u32 s9, s9, s11
	s_add_u32 s12, s12, s10
	s_addc_u32 s13, s13, s11
	s_add_i32 s14, s14, s3
	s_cmpk_lt_i32 s2, 0x2000
	s_waitcnt vmcnt(13)
	v_lshlrev_b32_e32 v97, 2, v98
	v_lshlrev_b32_e32 v98, 2, v99
	v_lshlrev_b32_e32 v99, 2, v100
	v_lshlrev_b32_e32 v100, 2, v101
	v_add_u32_e32 v97, s5, v97
	v_add_u32_e32 v101, s5, v98
	v_add_u32_e32 v99, s5, v99
	v_add_u32_e32 v105, s5, v100
	ds_read_b32 v98, v97
	ds_read_b32 v100, v101
	ds_read_b32 v108, v99
	ds_read_b32 v110, v105
	s_waitcnt vmcnt(12)
; __device__ __forceinline__ void p11_final(Frame& F, const Args& A) {
;     ...
;         for (int k = 0; k < 4; ++k) { const int e = WSP(int, WS_TOPI)[m * 4 + k], pos = WSP(int, WS_POS)[m * 4 + k]; p[k] = WSP(float, WS_TOPP)[m * 4 + k];
;             yr[k] = WSP(bf16, WS_YSLOT) + ((size_t)ts[e] * 256 + pos) * DM + 4 * F.lane; }
;         const float* hr = WSP(float, WS_H1) + (size_t)m * DM + 4 * F.lane; f32x4 v[8]; float s = 0.f;
; #pragma unroll
;         for (int j = 0; j < 8; ++j) { f32x4 a = {0.f, 0.f, 0.f, 0.f};
; #pragma unroll
;             for (int k = 0; k < 4; ++k) { const v2u w = *(const v2u*)(yr[k] + 256 * j); const f32x4 y = {__uint_as_float(w.x << 16), __uint_as_float(w.x & 0xffff0000u), __uint_as_float(w.y << 16), __uint_as_float(w.y & 0xffff0000u)}; a += y * p[k]; }
	v_ashrrev_i32_e32 v107, 31, v106
	s_waitcnt lgkmcnt(3)
	v_ashrrev_i32_e32 v99, 31, v98
	s_waitcnt lgkmcnt(2)
	v_ashrrev_i32_e32 v101, 31, v100
	s_waitcnt lgkmcnt(1)
	v_ashrrev_i32_e32 v109, 31, v108
	s_waitcnt lgkmcnt(0)
	v_ashrrev_i32_e32 v111, 31, v110
	v_lshlrev_b64 v[98:99], 20, v[98:99]
	v_lshlrev_b64 v[106:107], 12, v[106:107]
	s_waitcnt vmcnt(10)
	v_ashrrev_i32_e32 v113, 31, v102
	v_mov_b32_e32 v112, v102
	v_lshlrev_b64 v[100:101], 20, v[100:101]
	v_ashrrev_i32_e32 v115, 31, v103
	v_mov_b32_e32 v114, v103
	v_lshlrev_b64 v[102:103], 20, v[108:109]
	v_ashrrev_i32_e32 v105, 31, v104
	v_lshlrev_b64 v[108:109], 20, v[110:111]
	v_lshl_add_u64 v[98:99], s[6:7], 0, v[98:99]
	v_lshl_add_u64 v[100:101], s[6:7], 0, v[100:101]
	v_lshlrev_b64 v[110:111], 12, v[112:113]
	v_lshl_add_u64 v[102:103], s[6:7], 0, v[102:103]
	v_lshlrev_b64 v[112:113], 12, v[114:115]
	v_lshl_add_u64 v[108:109], s[6:7], 0, v[108:109]
	v_lshlrev_b64 v[104:105], 12, v[104:105]
	v_lshl_add_u64 v[98:99], v[98:99], 0, v[106:107]
	v_lshl_add_u64 v[100:101], v[100:101], 0, v[110:111]
	v_lshl_add_u64 v[102:103], v[102:103], 0, v[112:113]
	v_lshl_add_u64 v[104:105], v[108:109], 0, v[104:105]
	v_readfirstlane_b32 s0, v98
	v_readfirstlane_b32 s1, v99
	v_readfirstlane_b32 s34, v100
	v_readfirstlane_b32 s35, v101
	v_readfirstlane_b32 s36, v102
	v_readfirstlane_b32 s37, v103
	v_readfirstlane_b32 s38, v104
	v_readfirstlane_b32 s39, v105
	global_load_dwordx2 v[98:99], v94, s[0:1]
	global_load_dwordx2 v[100:101], v94, s[34:35]
	s_nop 0
	global_load_dwordx2 v[102:103], v94, s[36:37]
	s_nop 0
	global_load_dwordx2 v[104:105], v94, s[38:39]
	global_load_dwordx2 v[106:107], v94, s[0:1] offset:512
	global_load_dwordx2 v[108:109], v94, s[34:35] offset:512
	global_load_dwordx2 v[110:111], v94, s[36:37] offset:512
	global_load_dwordx2 v[112:113], v94, s[38:39] offset:512
	global_load_dwordx2 v[114:115], v94, s[0:1] offset:1024
	global_load_dwordx2 v[116:117], v94, s[34:35] offset:1024
	global_load_dwordx2 v[118:119], v94, s[36:37] offset:1024
	global_load_dwordx2 v[120:121], v94, s[38:39] offset:1024
	global_load_dwordx2 v[122:123], v94, s[0:1] offset:1536
	global_load_dwordx2 v[124:125], v94, s[34:35] offset:1536
	global_load_dwordx2 v[126:127], v94, s[36:37] offset:1536
	global_load_dwordx2 v[128:129], v94, s[38:39] offset:1536
	global_load_dwordx2 v[130:131], v94, s[0:1] offset:2048
	global_load_dwordx2 v[132:133], v94, s[0:1] offset:2560
	global_load_dwordx2 v[134:135], v94, s[0:1] offset:3072
	global_load_dwordx2 v[136:137], v94, s[0:1] offset:3584
	global_load_dwordx2 v[138:139], v94, s[34:35] offset:2048
	global_load_dwordx2 v[140:141], v94, s[34:35] offset:2560
	global_load_dwordx2 v[142:143], v94, s[34:35] offset:3072
	global_load_dwordx2 v[144:145], v94, s[34:35] offset:3584
	global_load_dwordx2 v[146:147], v94, s[36:37] offset:2048
	global_load_dwordx2 v[148:149], v94, s[36:37] offset:2560
	global_load_dwordx2 v[150:151], v94, s[36:37] offset:3072
	global_load_dwordx2 v[152:153], v94, s[36:37] offset:3584
	global_load_dwordx2 v[154:155], v94, s[38:39] offset:2048
	global_load_dwordx2 v[156:157], v94, s[38:39] offset:2560
	global_load_dwordx2 v[158:159], v94, s[38:39] offset:3072
	global_load_dwordx2 v[160:161], v94, s[38:39] offset:3584
	s_waitcnt vmcnt(31)
	v_lshlrev_b32_e32 v162, 16, v98
	v_and_b32_e32 v163, 0xffff0000, v98
	v_lshlrev_b32_e32 v98, 16, v99
	v_and_b32_e32 v99, 0xffff0000, v99
	s_waitcnt vmcnt(27)
	v_lshlrev_b32_e32 v170, 16, v106
	v_and_b32_e32 v171, 0xffff0000, v106
	v_lshlrev_b32_e32 v106, 16, v107
	v_and_b32_e32 v107, 0xffff0000, v107
	v_lshlrev_b32_e32 v164, 16, v100
	v_and_b32_e32 v165, 0xffff0000, v100
	v_lshlrev_b32_e32 v100, 16, v101
	v_and_b32_e32 v101, 0xffff0000, v101
	s_waitcnt vmcnt(26)
	v_lshlrev_b32_e32 v172, 16, v108
	v_and_b32_e32 v173, 0xffff0000, v108
	v_lshlrev_b32_e32 v108, 16, v109
	v_and_b32_e32 v109, 0xffff0000, v109
	s_waitcnt vmcnt(23)
	v_lshlrev_b32_e32 v178, 16, v114
	v_and_b32_e32 v179, 0xffff0000, v114
	v_lshlrev_b32_e32 v114, 16, v115
	v_and_b32_e32 v115, 0xffff0000, v115
	s_waitcnt vmcnt(19)
	v_lshlrev_b32_e32 v186, 16, v122
	v_and_b32_e32 v187, 0xffff0000, v122
	v_lshlrev_b32_e32 v122, 16, v123
	v_and_b32_e32 v123, 0xffff0000, v123
	s_waitcnt vmcnt(15)
	v_lshlrev_b32_e32 v194, 16, v130
	v_and_b32_e32 v195, 0xffff0000, v130
	v_lshlrev_b32_e32 v130, 16, v131
	v_and_b32_e32 v131, 0xffff0000, v131
	s_waitcnt vmcnt(14)
	v_lshlrev_b32_e32 v202, 16, v132
	v_and_b32_e32 v203, 0xffff0000, v132
	v_lshlrev_b32_e32 v132, 16, v133
	v_and_b32_e32 v133, 0xffff0000, v133
	s_waitcnt vmcnt(13)
	v_lshlrev_b32_e32 v210, 16, v134
	v_and_b32_e32 v211, 0xffff0000, v134
	v_lshlrev_b32_e32 v134, 16, v135
	v_and_b32_e32 v135, 0xffff0000, v135
	s_waitcnt vmcnt(12)
	v_lshlrev_b32_e32 v218, 16, v136
	v_and_b32_e32 v219, 0xffff0000, v136
	v_lshlrev_b32_e32 v136, 16, v137
	v_and_b32_e32 v137, 0xffff0000, v137
	v_pk_fma_f32 v[98:99], v[88:89], v[98:99], 0 op_sel_hi:[0,1,0]
	v_pk_fma_f32 v[162:163], v[88:89], v[162:163], 0 op_sel_hi:[0,1,0]
	v_pk_fma_f32 v[106:107], v[88:89], v[106:107], 0 op_sel_hi:[0,1,0]
	v_pk_fma_f32 v[170:171], v[88:89], v[170:171], 0 op_sel_hi:[0,1,0]
	v_lshlrev_b32_e32 v166, 16, v102
	v_and_b32_e32 v167, 0xffff0000, v102
	v_lshlrev_b32_e32 v102, 16, v103
	v_and_b32_e32 v103, 0xffff0000, v103
	v_lshlrev_b32_e32 v174, 16, v110
	v_and_b32_e32 v175, 0xffff0000, v110
	v_lshlrev_b32_e32 v110, 16, v111
	v_and_b32_e32 v111, 0xffff0000, v111
	v_lshlrev_b32_e32 v180, 16, v116
	v_and_b32_e32 v181, 0xffff0000, v116
	v_lshlrev_b32_e32 v116, 16, v117
	v_and_b32_e32 v117, 0xffff0000, v117
	v_lshlrev_b32_e32 v188, 16, v124
	v_and_b32_e32 v189, 0xffff0000, v124
	v_lshlrev_b32_e32 v124, 16, v125
	v_and_b32_e32 v125, 0xffff0000, v125
	s_waitcnt vmcnt(11)
; __device__ __forceinline__ void p11_final(Frame& F, const Args& A) {
;     ...
;         for (int j = 0; j < 8; ++j) { f32x4 a = {0.f, 0.f, 0.f, 0.f};
; #pragma unroll
;             for (int k = 0; k < 4; ++k) { const v2u w = *(const v2u*)(yr[k] + 256 * j); const f32x4 y = {__uint_as_float(w.x << 16), __uint_as_float(w.x & 0xffff0000u), __uint_as_float(w.y << 16), __uint_as_float(w.y & 0xffff0000u)}; a += y * p[k]; }
	v_lshlrev_b32_e32 v196, 16, v138
	v_and_b32_e32 v197, 0xffff0000, v138
	v_lshlrev_b32_e32 v138, 16, v139
	v_and_b32_e32 v139, 0xffff0000, v139
	s_waitcnt vmcnt(10)
	v_lshlrev_b32_e32 v204, 16, v140
	v_and_b32_e32 v205, 0xffff0000, v140
	v_lshlrev_b32_e32 v140, 16, v141
	v_and_b32_e32 v141, 0xffff0000, v141
	s_waitcnt vmcnt(9)
	v_lshlrev_b32_e32 v212, 16, v142
	v_and_b32_e32 v213, 0xffff0000, v142
	v_lshlrev_b32_e32 v142, 16, v143
	v_and_b32_e32 v143, 0xffff0000, v143
	s_waitcnt vmcnt(8)
	v_lshlrev_b32_e32 v220, 16, v144
	v_and_b32_e32 v221, 0xffff0000, v144
	v_lshlrev_b32_e32 v144, 16, v145
	v_and_b32_e32 v145, 0xffff0000, v145
	v_pk_fma_f32 v[178:179], v[88:89], v[178:179], 0 op_sel_hi:[0,1,0]
	v_pk_fma_f32 v[114:115], v[88:89], v[114:115], 0 op_sel_hi:[0,1,0]
	v_pk_fma_f32 v[122:123], v[88:89], v[122:123], 0 op_sel_hi:[0,1,0]
	v_pk_fma_f32 v[186:187], v[88:89], v[186:187], 0 op_sel_hi:[0,1,0]
	v_pk_fma_f32 v[130:131], v[88:89], v[130:131], 0 op_sel_hi:[0,1,0]
	v_pk_fma_f32 v[194:195], v[88:89], v[194:195], 0 op_sel_hi:[0,1,0]
	v_pk_fma_f32 v[202:203], v[88:89], v[202:203], 0 op_sel_hi:[0,1,0]
	v_pk_fma_f32 v[132:133], v[88:89], v[132:133], 0 op_sel_hi:[0,1,0]
	v_pk_fma_f32 v[134:135], v[88:89], v[134:135], 0 op_sel_hi:[0,1,0]
	v_pk_fma_f32 v[210:211], v[88:89], v[210:211], 0 op_sel_hi:[0,1,0]
	v_pk_fma_f32 v[136:137], v[88:89], v[136:137], 0 op_sel_hi:[0,1,0]
	v_pk_fma_f32 v[218:219], v[88:89], v[218:219], 0 op_sel_hi:[0,1,0]
	v_pk_fma_f32 v[162:163], v[86:87], v[164:165], v[162:163] op_sel_hi:[0,1,1]
	v_pk_fma_f32 v[98:99], v[86:87], v[100:101], v[98:99] op_sel_hi:[0,1,1]
	v_pk_fma_f32 v[100:101], v[86:87], v[172:173], v[170:171] op_sel_hi:[0,1,1]
	v_pk_fma_f32 v[106:107], v[86:87], v[108:109], v[106:107] op_sel_hi:[0,1,1]
	v_lshlrev_b32_e32 v168, 16, v104
	v_and_b32_e32 v169, 0xffff0000, v104
	v_lshlrev_b32_e32 v104, 16, v105
	v_and_b32_e32 v105, 0xffff0000, v105
	v_lshlrev_b32_e32 v176, 16, v112
	v_and_b32_e32 v177, 0xffff0000, v112
	v_lshlrev_b32_e32 v112, 16, v113
	v_and_b32_e32 v113, 0xffff0000, v113
	v_lshlrev_b32_e32 v182, 16, v118
	v_and_b32_e32 v183, 0xffff0000, v118
	v_lshlrev_b32_e32 v118, 16, v119
	v_and_b32_e32 v119, 0xffff0000, v119
	v_lshlrev_b32_e32 v190, 16, v126
	v_and_b32_e32 v191, 0xffff0000, v126
	v_lshlrev_b32_e32 v126, 16, v127
	v_and_b32_e32 v127, 0xffff0000, v127
	s_waitcnt vmcnt(7)
	v_lshlrev_b32_e32 v198, 16, v146
	v_and_b32_e32 v199, 0xffff0000, v146
	v_lshlrev_b32_e32 v146, 16, v147
	v_and_b32_e32 v147, 0xffff0000, v147
	s_waitcnt vmcnt(6)
	v_lshlrev_b32_e32 v206, 16, v148
	v_and_b32_e32 v207, 0xffff0000, v148
	v_lshlrev_b32_e32 v148, 16, v149
	v_and_b32_e32 v149, 0xffff0000, v149
	s_waitcnt vmcnt(5)
	v_lshlrev_b32_e32 v214, 16, v150
	v_and_b32_e32 v215, 0xffff0000, v150
	v_lshlrev_b32_e32 v150, 16, v151
	v_and_b32_e32 v151, 0xffff0000, v151
	s_waitcnt vmcnt(4)
	v_lshlrev_b32_e32 v222, 16, v152
	v_and_b32_e32 v223, 0xffff0000, v152
	v_lshlrev_b32_e32 v152, 16, v153
	v_and_b32_e32 v153, 0xffff0000, v153
	v_pk_fma_f32 v[108:109], v[86:87], v[116:117], v[114:115] op_sel_hi:[0,1,1]
	v_pk_fma_f32 v[114:115], v[86:87], v[180:181], v[178:179] op_sel_hi:[0,1,1]
	v_pk_fma_f32 v[116:117], v[86:87], v[188:189], v[186:187] op_sel_hi:[0,1,1]
	v_pk_fma_f32 v[122:123], v[86:87], v[124:125], v[122:123] op_sel_hi:[0,1,1]
	v_pk_fma_f32 v[124:125], v[86:87], v[196:197], v[194:195] op_sel_hi:[0,1,1]
	v_pk_fma_f32 v[130:131], v[86:87], v[138:139], v[130:131] op_sel_hi:[0,1,1]
	v_pk_fma_f32 v[132:133], v[86:87], v[140:141], v[132:133] op_sel_hi:[0,1,1]
	v_pk_fma_f32 v[138:139], v[86:87], v[204:205], v[202:203] op_sel_hi:[0,1,1]
	v_pk_fma_f32 v[140:141], v[86:87], v[212:213], v[210:211] op_sel_hi:[0,1,1]
	v_pk_fma_f32 v[134:135], v[86:87], v[142:143], v[134:135] op_sel_hi:[0,1,1]
	v_pk_fma_f32 v[142:143], v[86:87], v[220:221], v[218:219] op_sel_hi:[0,1,1]
	v_pk_fma_f32 v[136:137], v[86:87], v[144:145], v[136:137] op_sel_hi:[0,1,1]
	v_pk_fma_f32 v[98:99], v[84:85], v[102:103], v[98:99] op_sel_hi:[0,1,1]
	v_pk_fma_f32 v[102:103], v[84:85], v[166:167], v[162:163] op_sel_hi:[0,1,1]
	v_pk_fma_f32 v[106:107], v[84:85], v[110:111], v[106:107] op_sel_hi:[0,1,1]
	v_pk_fma_f32 v[100:101], v[84:85], v[174:175], v[100:101] op_sel_hi:[0,1,1]
	v_lshlrev_b32_e32 v184, 16, v120
	v_and_b32_e32 v185, 0xffff0000, v120
	v_lshlrev_b32_e32 v120, 16, v121
	v_and_b32_e32 v121, 0xffff0000, v121
	v_lshlrev_b32_e32 v192, 16, v128
	v_and_b32_e32 v193, 0xffff0000, v128
	v_lshlrev_b32_e32 v128, 16, v129
	v_and_b32_e32 v129, 0xffff0000, v129
	s_waitcnt vmcnt(3)
	v_lshlrev_b32_e32 v200, 16, v154
	v_and_b32_e32 v201, 0xffff0000, v154
	v_lshlrev_b32_e32 v154, 16, v155
	v_and_b32_e32 v155, 0xffff0000, v155
	s_waitcnt vmcnt(2)
	v_lshlrev_b32_e32 v208, 16, v156
	v_and_b32_e32 v209, 0xffff0000, v156
	v_lshlrev_b32_e32 v156, 16, v157
	v_and_b32_e32 v157, 0xffff0000, v157
	s_waitcnt vmcnt(1)
	v_lshlrev_b32_e32 v216, 16, v158
	v_and_b32_e32 v217, 0xffff0000, v158
	v_lshlrev_b32_e32 v158, 16, v159
	v_and_b32_e32 v159, 0xffff0000, v159
	s_waitcnt vmcnt(0)
; __device__ __forceinline__ void p11_final(Frame& F, const Args& A) {
;     ...
;             for (int k = 0; k < 4; ++k) { const v2u w = *(const v2u*)(yr[k] + 256 * j); const f32x4 y = {__uint_as_float(w.x << 16), __uint_as_float(w.x & 0xffff0000u), __uint_as_float(w.y << 16), __uint_as_float(w.y & 0xffff0000u)}; a += y * p[k]; }
;             const f32x4 g2 = *(const f32x4*)(MODp + bb * 12288 + 5 * DM + 4 * F.lane + 256 * j);
;             v[j] = *(const f32x4*)(hr + 256 * j) + g2 * a; s += (v[j].x * v[j].x + v[j].y * v[j].y) + (v[j].z * v[j].z + v[j].w * v[j].w); }
;         const float rstd = 1.0f / sqrtf(wave_sum(s) * (1.0f / DM) + EPS);
	v_lshlrev_b32_e32 v224, 16, v160
	v_and_b32_e32 v225, 0xffff0000, v160
	v_lshlrev_b32_e32 v160, 16, v161
	v_and_b32_e32 v161, 0xffff0000, v161
	v_pk_fma_f32 v[110:111], v[84:85], v[182:183], v[114:115] op_sel_hi:[0,1,1]
	v_pk_fma_f32 v[108:109], v[84:85], v[118:119], v[108:109] op_sel_hi:[0,1,1]
	v_pk_fma_f32 v[114:115], v[84:85], v[126:127], v[122:123] op_sel_hi:[0,1,1]
	v_pk_fma_f32 v[116:117], v[84:85], v[190:191], v[116:117] op_sel_hi:[0,1,1]
	v_pk_fma_f32 v[118:119], v[84:85], v[146:147], v[130:131] op_sel_hi:[0,1,1]
	v_pk_fma_f32 v[122:123], v[84:85], v[198:199], v[124:125] op_sel_hi:[0,1,1]
	v_pk_fma_f32 v[124:125], v[84:85], v[206:207], v[138:139] op_sel_hi:[0,1,1]
	v_pk_fma_f32 v[126:127], v[84:85], v[148:149], v[132:133] op_sel_hi:[0,1,1]
	v_pk_fma_f32 v[130:131], v[84:85], v[150:151], v[134:135] op_sel_hi:[0,1,1]
	v_pk_fma_f32 v[132:133], v[84:85], v[214:215], v[140:141] op_sel_hi:[0,1,1]
	v_pk_fma_f32 v[134:135], v[84:85], v[152:153], v[136:137] op_sel_hi:[0,1,1]
	v_pk_fma_f32 v[136:137], v[84:85], v[222:223], v[142:143] op_sel_hi:[0,1,1]
	v_pk_fma_f32 v[102:103], v[84:85], v[168:169], v[102:103] op_sel:[1,0,0]
	v_pk_fma_f32 v[98:99], v[84:85], v[104:105], v[98:99] op_sel:[1,0,0]
	v_pk_fma_f32 v[100:101], v[84:85], v[176:177], v[100:101] op_sel:[1,0,0]
	v_pk_fma_f32 v[104:105], v[84:85], v[112:113], v[106:107] op_sel:[1,0,0]
	v_pk_fma_f32 v[106:107], v[84:85], v[120:121], v[108:109] op_sel:[1,0,0]
	v_pk_fma_f32 v[108:109], v[84:85], v[184:185], v[110:111] op_sel:[1,0,0]
	v_pk_fma_f32 v[110:111], v[84:85], v[192:193], v[116:117] op_sel:[1,0,0]
	v_pk_fma_f32 v[112:113], v[84:85], v[128:129], v[114:115] op_sel:[1,0,0]
	v_pk_fma_f32 v[114:115], v[84:85], v[200:201], v[122:123] op_sel:[1,0,0]
	v_pk_fma_f32 v[116:117], v[84:85], v[154:155], v[118:119] op_sel:[1,0,0]
	v_pk_fma_f32 v[118:119], v[84:85], v[156:157], v[126:127] op_sel:[1,0,0]
	v_pk_fma_f32 v[120:121], v[84:85], v[208:209], v[124:125] op_sel:[1,0,0]
	v_pk_fma_f32 v[122:123], v[84:85], v[216:217], v[132:133] op_sel:[1,0,0]
	v_pk_fma_f32 v[124:125], v[84:85], v[158:159], v[130:131] op_sel:[1,0,0]
	v_pk_fma_f32 v[126:127], v[84:85], v[224:225], v[136:137] op_sel:[1,0,0]
	v_pk_fma_f32 v[84:85], v[84:85], v[160:161], v[134:135] op_sel:[1,0,0]
	v_pk_fma_f32 v[34:35], v[66:67], v[98:99], v[34:35]
	v_pk_fma_f32 v[32:33], v[64:65], v[102:103], v[32:33]
	v_pk_fma_f32 v[30:31], v[62:63], v[104:105], v[30:31]
	v_pk_fma_f32 v[28:29], v[60:61], v[100:101], v[28:29]
	v_pk_fma_f32 v[24:25], v[56:57], v[108:109], v[24:25]
	v_pk_fma_f32 v[26:27], v[58:59], v[106:107], v[26:27]
	v_pk_fma_f32 v[10:11], v[42:43], v[124:125], v[10:11]
	v_pk_fma_f32 v[6:7], v[38:39], v[84:85], v[6:7]
	v_mov_b32_e32 v38, v33
	v_mov_b32_e32 v39, v29
	v_mov_b32_e32 v42, v35
	v_mov_b32_e32 v43, v31
	v_pk_fma_f32 v[12:13], v[44:45], v[120:121], v[12:13]
	v_pk_fma_f32 v[14:15], v[46:47], v[118:119], v[14:15]
	v_pk_fma_f32 v[8:9], v[40:41], v[122:123], v[8:9]
	v_pk_fma_f32 v[4:5], v[36:37], v[126:127], v[4:5]
	v_mov_b32_e32 v36, v32
	v_mov_b32_e32 v37, v28
	v_mov_b32_e32 v40, v34
	v_mov_b32_e32 v41, v30
	v_pk_mul_f32 v[44:45], v[26:27], v[26:27]
	v_pk_mul_f32 v[46:47], v[24:25], v[24:25]
	v_pk_mul_f32 v[38:39], v[38:39], v[38:39]
	v_pk_mul_f32 v[42:43], v[42:43], v[42:43]
	v_pk_fma_f32 v[18:19], v[50:51], v[112:113], v[18:19]
	v_pk_fma_f32 v[16:17], v[48:49], v[110:111], v[16:17]
	v_pk_mov_b32 v[60:61], v[46:47], v[44:45] op_sel:[1,0]
	v_mov_b32_e32 v47, v45
	v_pk_fma_f32 v[36:37], v[36:37], v[36:37], v[38:39]
	v_pk_fma_f32 v[38:39], v[40:41], v[40:41], v[42:43]
	v_pk_fma_f32 v[22:23], v[54:55], v[116:117], v[22:23]
	v_pk_fma_f32 v[20:21], v[52:53], v[114:115], v[20:21]
	v_mul_f32_e32 v48, v17, v17
	v_mul_f32_e32 v50, v19, v19
	v_pk_add_f32 v[40:41], v[60:61], v[46:47]
	v_pk_add_f32 v[36:37], v[36:37], v[38:39]
	v_mul_f32_e32 v59, v20, v20
	v_mul_f32_e32 v62, v21, v21
	v_mul_f32_e32 v63, v22, v22
	v_mul_f32_e32 v64, v23, v23
	v_pk_fma_f32 v[44:45], v[16:17], v[16:17], v[48:49] op_sel_hi:[1,1,0]
	v_pk_fma_f32 v[48:49], v[18:19], v[18:19], v[50:51] op_sel_hi:[1,1,0]
	v_pk_add_f32 v[38:39], v[40:41], v[40:41] op_sel:[0,1] op_sel_hi:[1,0]
	v_pk_add_f32 v[36:37], v[36:37], v[36:37] op_sel:[0,1] op_sel_hi:[1,0]
	v_pk_mul_f32 v[52:53], v[14:15], v[14:15]
	v_pk_mul_f32 v[54:55], v[12:13], v[12:13]
	v_mov_b32_e32 v45, v63
	v_mov_b32_e32 v49, v64
	v_mov_b32_e32 v39, v62
	v_mov_b32_e32 v37, v59
	v_pk_mov_b32 v[50:51], v[54:55], v[52:53] op_sel:[1,0]
	v_mov_b32_e32 v55, v53
	v_pk_add_f32 v[40:41], v[44:45], v[48:49]
	v_pk_add_f32 v[36:37], v[36:37], v[38:39]
	v_mul_f32_e32 v56, v9, v9
	v_mul_f32_e32 v58, v11, v11
	v_pk_add_f32 v[42:43], v[50:51], v[54:55]
	v_pk_add_f32 v[36:37], v[36:37], v[40:41]
	v_mul_f32_e32 v65, v4, v4
	v_mul_f32_e32 v66, v5, v5
	v_mul_f32_e32 v67, v6, v6
	v_mul_f32_e32 v84, v7, v7
	v_pk_fma_f32 v[52:53], v[8:9], v[8:9], v[56:57] op_sel_hi:[1,1,0]
	v_pk_fma_f32 v[56:57], v[10:11], v[10:11], v[58:59] op_sel_hi:[1,1,0]
	v_pk_add_f32 v[42:43], v[42:43], v[42:43] op_sel:[0,1] op_sel_hi:[1,0]
	v_pk_add_f32 v[36:37], v[36:37], v[36:37] op_sel:[0,1] op_sel_hi:[1,0]
	v_mov_b32_e32 v53, v67
	v_mov_b32_e32 v57, v84
	v_mov_b32_e32 v43, v66
	v_mov_b32_e32 v37, v65
	v_pk_add_f32 v[44:45], v[52:53], v[56:57]
	v_pk_add_f32 v[36:37], v[36:37], v[42:43]
	s_nop 0
	v_pk_add_f32 v[36:37], v[36:37], v[44:45]
	s_nop 0
	v_add_f32_e32 v36, v36, v37
	ds_bpermute_b32 v37, v87, v36
	s_waitcnt lgkmcnt(0)
; __device__ __forceinline__ void p11_final(Frame& F, const Args& A) {
;     ...
;         const float rstd = 1.0f / sqrtf(wave_sum(s) * (1.0f / DM) + EPS);
;         float* orow = A.out + (size_t)m * DM + 4 * F.lane;
; #pragma unroll
;         for (int j = 0; j < 8; ++j) { const f32x4 g = *(const f32x4*)(A.in[I_FG] + 4 * F.lane + 256 * j); *(f32x4*)(orow + 256 * j) = v[j] * rstd * g; }
	v_add_f32_e32 v36, v36, v37
	ds_bpermute_b32 v37, v89, v36
	s_waitcnt lgkmcnt(0)
	v_add_f32_e32 v36, v36, v37
	ds_bpermute_b32 v37, v90, v36
	s_waitcnt lgkmcnt(0)
	v_add_f32_e32 v36, v36, v37
	ds_bpermute_b32 v37, v91, v36
	s_waitcnt lgkmcnt(0)
	v_add_f32_e32 v36, v36, v37
	ds_bpermute_b32 v37, v92, v36
	s_waitcnt lgkmcnt(0)
	v_add_f32_e32 v36, v36, v37
	ds_bpermute_b32 v37, v93, v36
	s_waitcnt lgkmcnt(0)
	v_add_f32_e32 v36, v36, v37
	v_fmamk_f32 v36, v36, 0x3a000000, v95
	v_mul_f32_e32 v37, 0x4f800000, v36
	v_cmp_gt_f32_e32 vcc, s27, v36
	s_nop 1
	v_cndmask_b32_e32 v36, v36, v37, vcc
	v_sqrt_f32_e32 v37, v36
	s_nop 0
	v_add_u32_e32 v38, -1, v37
	v_add_u32_e32 v39, 1, v37
	v_fma_f32 v40, -v38, v37, v36
	v_fma_f32 v41, -v39, v37, v36
	v_cmp_ge_f32_e64 s[0:1], 0, v40
	s_nop 1
	v_cndmask_b32_e64 v37, v37, v38, s[0:1]
	v_cmp_lt_f32_e64 s[0:1], 0, v41
	s_nop 1
	v_cndmask_b32_e64 v37, v37, v39, s[0:1]
	v_mul_f32_e32 v38, 0x37800000, v37
	v_cndmask_b32_e32 v37, v37, v38, vcc
	v_cmp_class_f32_e32 vcc, v36, v96
	s_nop 1
	v_cndmask_b32_e32 v36, v37, v36, vcc
	v_div_scale_f32 v37, s[0:1], v36, v36, 1.0
	v_rcp_f32_e32 v39, v37
	v_div_scale_f32 v38, vcc, 1.0, v36, 1.0
	v_fma_f32 v40, -v37, v39, 1.0
	v_fmac_f32_e32 v39, v40, v39
	v_mul_f32_e32 v40, v38, v39
	v_fma_f32 v41, -v37, v40, v38
	v_fmac_f32_e32 v40, v41, v39
	v_fma_f32 v37, -v37, v40, v38
	v_div_fmas_f32 v37, v37, v39, v40
	v_div_fixup_f32 v36, v37, v36, 1.0
	v_pk_mul_f32 v[32:33], v[32:33], v[36:37] op_sel_hi:[1,0]
	v_pk_mul_f32 v[34:35], v[34:35], v[36:37] op_sel_hi:[1,0]
	v_pk_mul_f32 v[28:29], v[28:29], v[36:37] op_sel_hi:[1,0]
	v_pk_mul_f32 v[30:31], v[30:31], v[36:37] op_sel_hi:[1,0]
	v_pk_mul_f32 v[24:25], v[24:25], v[36:37] op_sel_hi:[1,0]
	v_pk_mul_f32 v[26:27], v[26:27], v[36:37] op_sel_hi:[1,0]
	v_pk_mul_f32 v[16:17], v[16:17], v[36:37] op_sel_hi:[1,0]
	v_pk_mul_f32 v[18:19], v[18:19], v[36:37] op_sel_hi:[1,0]
	v_pk_mul_f32 v[20:21], v[20:21], v[36:37] op_sel_hi:[1,0]
	v_pk_mul_f32 v[22:23], v[22:23], v[36:37] op_sel_hi:[1,0]
	v_pk_mul_f32 v[12:13], v[12:13], v[36:37] op_sel_hi:[1,0]
	v_pk_mul_f32 v[14:15], v[14:15], v[36:37] op_sel_hi:[1,0]
	v_pk_mul_f32 v[8:9], v[8:9], v[36:37] op_sel_hi:[1,0]
	v_pk_mul_f32 v[10:11], v[10:11], v[36:37] op_sel_hi:[1,0]
	v_pk_mul_f32 v[4:5], v[4:5], v[36:37] op_sel_hi:[1,0]
	v_pk_mul_f32 v[6:7], v[6:7], v[36:37] op_sel_hi:[1,0]
	v_pk_mul_f32 v[32:33], v[226:227], v[32:33]
	v_pk_mul_f32 v[34:35], v[228:229], v[34:35]
	global_store_dwordx4 v[82:83], v[32:35], off
	v_pk_mul_f32 v[28:29], v[230:231], v[28:29]
	v_pk_mul_f32 v[30:31], v[232:233], v[30:31]
	global_store_dwordx4 v[82:83], v[28:31], off offset:1024
	v_pk_mul_f32 v[24:25], v[234:235], v[24:25]
	v_pk_mul_f32 v[26:27], v[236:237], v[26:27]
	global_store_dwordx4 v[82:83], v[24:27], off offset:2048
	v_pk_mul_f32 v[16:17], v[238:239], v[16:17]
	v_pk_mul_f32 v[18:19], v[240:241], v[18:19]
	global_store_dwordx4 v[82:83], v[16:19], off offset:3072
	v_add_co_u32_e32 v98, vcc, s28, v82
	s_nop 1
	v_addc_co_u32_e32 v99, vcc, 0, v83, vcc
	v_pk_mul_f32 v[20:21], v[242:243], v[20:21]
	v_pk_mul_f32 v[22:23], v[244:245], v[22:23]
	global_store_dwordx4 v[98:99], v[20:23], off
	v_pk_mul_f32 v[12:13], v[248:249], v[12:13]
	v_pk_mul_f32 v[14:15], v[250:251], v[14:15]
	global_store_dwordx4 v[98:99], v[12:15], off offset:1024
	v_pk_mul_f32 v[8:9], v[252:253], v[8:9]
	v_pk_mul_f32 v[10:11], v[254:255], v[10:11]
	global_store_dwordx4 v[98:99], v[8:11], off offset:2048
	v_pk_mul_f32 v[4:5], v[0:1], v[4:5]
	v_pk_mul_f32 v[6:7], v[2:3], v[6:7]
	global_store_dwordx4 v[98:99], v[4:7], off offset:3072
	s_cbranch_scc1 .LBB0_1149

; __global__ void __launch_bounds__(NWAVES * 64, 2) fwd(Args args) {
	.amdhsa_kernel _Z3fwd4Args
		.amdhsa_group_segment_fixed_size 0
		.amdhsa_private_segment_fixed_size 0
		.amdhsa_kernarg_size 472
		.amdhsa_user_sgpr_count 2
		.amdhsa_user_sgpr_dispatch_ptr 0
		.amdhsa_user_sgpr_queue_ptr 0
		.amdhsa_user_sgpr_kernarg_segment_ptr 1
		.amdhsa_user_sgpr_dispatch_id 0
		.amdhsa_user_sgpr_kernarg_preload_length 0
		.amdhsa_user_sgpr_kernarg_preload_offset 0
		.amdhsa_user_sgpr_private_segment_size 0
		.amdhsa_uses_dynamic_stack 0
		.amdhsa_enable_private_segment 0
		.amdhsa_system_sgpr_workgroup_id_x 1
		.amdhsa_system_sgpr_workgroup_id_y 0
		.amdhsa_system_sgpr_workgroup_id_z 0
		.amdhsa_system_sgpr_workgroup_info 0
		.amdhsa_system_vgpr_workitem_id 0
		.amdhsa_next_free_vgpr 256
		.amdhsa_next_free_sgpr 98
		.amdhsa_accum_offset 256
		.amdhsa_reserve_vcc 1
		.amdhsa_float_round_mode_32 0
		.amdhsa_float_round_mode_16_64 0
		.amdhsa_float_denorm_mode_32 3
		.amdhsa_float_denorm_mode_16_64 3
		.amdhsa_dx10_clamp 1
		.amdhsa_ieee_mode 1
		.amdhsa_fp16_overflow 0
		.amdhsa_tg_split 0
		.amdhsa_exception_fp_ieee_invalid_op 0
		.amdhsa_exception_fp_denorm_src 0
		.amdhsa_exception_fp_ieee_div_zero 0
		.amdhsa_exception_fp_ieee_overflow 0
		.amdhsa_exception_fp_ieee_underflow 0
		.amdhsa_exception_fp_ieee_inexact 0
		.amdhsa_exception_int_div_zero 0
	.end_amdhsa_kernel

; __global__ void __launch_bounds__(NWAVES * 64, 2) fwd(Args args) {
amdhsa.kernels:
  - .agpr_count:     0
    .args:
      - .offset:         0
        .size:           216
        .value_kind:     by_value
      - .offset:         216
        .size:           4
        .value_kind:     hidden_block_count_x
      - .offset:         220
        .size:           4
        .value_kind:     hidden_block_count_y
      - .offset:         224
        .size:           4
        .value_kind:     hidden_block_count_z
      - .offset:         228
        .size:           2
        .value_kind:     hidden_group_size_x
      - .offset:         230
        .size:           2
        .value_kind:     hidden_group_size_y
      - .offset:         232
        .size:           2
        .value_kind:     hidden_group_size_z
      - .offset:         234
        .size:           2
        .value_kind:     hidden_remainder_x
      - .offset:         236
        .size:           2
        .value_kind:     hidden_remainder_y
      - .offset:         238
        .size:           2
        .value_kind:     hidden_remainder_z
      - .offset:         256
        .size:           8
        .value_kind:     hidden_global_offset_x
      - .offset:         264
        .size:           8
        .value_kind:     hidden_global_offset_y
      - .offset:         272
        .size:           8
        .value_kind:     hidden_global_offset_z
      - .offset:         280
        .size:           2
        .value_kind:     hidden_grid_dims
      - .offset:         336
        .size:           4
        .value_kind:     hidden_dynamic_lds_size
    .group_segment_fixed_size: 0
    .kernarg_segment_align: 8
    .kernarg_segment_size: 472
    .language:       OpenCL C
    .language_version:
      - 2
      - 0
    .max_flat_workgroup_size: 512
    .name:           _Z3fwd4Args
    .private_segment_fixed_size: 0
    .sgpr_count:     104
    .sgpr_spill_count: 58
    .symbol:         _Z3fwd4Args.kd
    .uniform_work_group_size: 1
    .uses_dynamic_stack: false
    .vgpr_count:     256
    .vgpr_spill_count: 0
    .wavefront_size: 64
